# v17 + dilated attention: waves 4-7 start each unit's item loop ~2k cycles later (stagger the two waves of a SIMD)
# speedup vs baseline: 1.0261x; 1.0261x over previous
.LBB0_195:
	v_add_u32_e32 v0, s49, v225
	v_add_u32_e32 v6, v0, v227
	v_add_u32_e32 v7, v0, v228
	ds_read_b128 v[244:247], v6
	ds_read_b128 v[248:251], v6 offset:8192
	ds_read_b128 v[236:239], v7
	ds_read_b128 v[208:211], v7 offset:8192
	v_add_u32_e32 v6, v0, v229
	v_add_u32_e32 v7, v0, v230
	ds_read_b128 v[2:5], v6
	ds_read_b128 v[8:11], v6 offset:8192
	ds_read_b128 v[12:15], v7
	s_xor_b64 s[44:45], s[44:45], -1
	v_add_u32_e32 v6, v0, v226
	s_waitcnt lgkmcnt(6)
	v_mfma_f32_32x32x16_bf16 v[144:159], v[244:247], v[176:179], v[144:159]
	ds_read_b128 v[244:247], v7 offset:8192
	s_waitcnt lgkmcnt(6)
	v_mfma_f32_32x32x16_bf16 v[160:175], v[248:251], v[176:179], v[160:175]
	s_waitcnt lgkmcnt(5)
	v_mfma_f32_32x32x16_bf16 v[144:159], v[236:239], v[180:183], v[144:159]
	ds_read_b128 v[248:251], v6
	ds_read_b128 v[236:239], v6 offset:8192
	s_waitcnt lgkmcnt(6)
	v_mfma_f32_32x32x16_bf16 v[160:175], v[208:211], v[180:183], v[160:175]
	v_add_u32_e32 v7, v0, v231
	s_waitcnt lgkmcnt(5)
	v_mfma_f32_32x32x16_bf16 v[144:159], v[2:5], v[184:187], v[144:159]
	s_waitcnt lgkmcnt(4)
	v_mfma_f32_32x32x16_bf16 v[160:175], v[8:11], v[184:187], v[160:175]
	s_waitcnt lgkmcnt(3)
	v_mfma_f32_32x32x16_bf16 v[144:159], v[12:15], v[188:191], v[144:159]
	s_waitcnt lgkmcnt(2)
	v_mfma_f32_32x32x16_bf16 v[160:175], v[244:247], v[188:191], v[160:175]
	ds_read_b128 v[244:247], v7
	s_nop 9
	v_exp_f32_e32 v6, v144
	v_exp_f32_e32 v3, v145
	v_exp_f32_e32 v10, v148
	v_exp_f32_e32 v11, v149
	v_exp_f32_e32 v12, v150
	v_exp_f32_e32 v148, v152
	v_exp_f32_e32 v150, v153
	v_exp_f32_e32 v156, v156
	v_exp_f32_e32 v157, v157
	v_exp_f32_e32 v5, v146
	v_exp_f32_e32 v152, v154
	v_exp_f32_e32 v158, v158
	v_exp_f32_e32 v8, v147
	v_exp_f32_e32 v13, v151
	v_exp_f32_e32 v154, v155
	v_exp_f32_e32 v159, v159
	v_exp_f32_e32 v2, v160
	v_exp_f32_e32 v144, v164
	v_exp_f32_e32 v149, v168
	v_exp_f32_e32 v160, v172
	v_exp_f32_e32 v4, v161
	v_exp_f32_e32 v145, v165
	v_exp_f32_e32 v151, v169
	v_exp_f32_e32 v161, v173
	v_add_f32_e32 v14, v6, v3
	v_add_f32_e32 v15, v10, v11
	v_add_f32_e32 v164, v148, v150
	v_add_f32_e32 v165, v156, v157
	v_exp_f32_e32 v7, v162
	v_exp_f32_e32 v146, v166
	v_exp_f32_e32 v153, v170
	v_exp_f32_e32 v162, v174
	v_add_f32_e32 v14, v5, v14
	v_add_f32_e32 v15, v12, v15
	v_add_f32_e32 v164, v152, v164
	v_add_f32_e32 v165, v158, v165
	v_exp_f32_e32 v9, v163
	v_exp_f32_e32 v147, v167
	v_exp_f32_e32 v155, v171
	v_exp_f32_e32 v163, v175
	v_add_f32_e32 v14, v8, v14
	v_add_f32_e32 v15, v13, v15
	v_add_f32_e32 v164, v154, v164
	v_add_f32_e32 v165, v159, v165
	v_add_f32_e32 v14, v2, v14
	v_add_f32_e32 v15, v144, v15
	v_add_f32_e32 v164, v149, v164
	v_add_f32_e32 v165, v160, v165
	v_add_f32_e32 v14, v4, v14
	v_add_f32_e32 v15, v145, v15
	v_add_f32_e32 v164, v151, v164
	v_add_f32_e32 v165, v161, v165
	v_add_f32_e32 v14, v7, v14
	v_add_f32_e32 v15, v146, v15
	v_add_f32_e32 v164, v153, v164
	v_add_f32_e32 v165, v162, v165
	v_add_f32_e32 v14, v9, v14
	v_add_f32_e32 v15, v147, v15
	v_add_f32_e32 v164, v155, v164
	v_add_f32_e32 v165, v163, v165
	v_add_f32_e32 v14, v14, v15
	v_add_f32_e32 v15, v164, v165
	v_add_f32_e32 v14, v14, v15
	v_mov_b32_e32 v15, v14
	v_cvt_pk_bf16_f32 v208, v6, v3
	v_cvt_pk_bf16_f32 v209, v5, v8
	v_cvt_pk_bf16_f32 v210, v10, v11
	v_cvt_pk_bf16_f32 v211, v12, v13
	v_cvt_pk_bf16_f32 v10, v148, v150
	v_cvt_pk_bf16_f32 v11, v152, v154
	v_cvt_pk_bf16_f32 v12, v156, v157
	v_cvt_pk_bf16_f32 v13, v158, v159
	v_cvt_pk_bf16_f32 v6, v2, v4
	v_cvt_pk_bf16_f32 v7, v7, v9
	v_cvt_pk_bf16_f32 v8, v144, v145
	v_cvt_pk_bf16_f32 v9, v146, v147
	v_cvt_pk_bf16_f32 v2, v149, v151
	v_cvt_pk_bf16_f32 v3, v153, v155
	v_cvt_pk_bf16_f32 v4, v160, v161
	v_cvt_pk_bf16_f32 v5, v162, v163
	v_permlane32_swap_b32_e32 v14, v15
	v_permlane32_swap_b32_e32 v208, v210
	v_permlane32_swap_b32_e32 v209, v211
	v_permlane32_swap_b32_e32 v10, v12
	v_permlane32_swap_b32_e32 v11, v13
	v_permlane32_swap_b32_e32 v6, v8
	v_permlane32_swap_b32_e32 v7, v9
	v_permlane32_swap_b32_e32 v2, v4
	v_permlane32_swap_b32_e32 v3, v5
	s_nop 15
	s_nop 15
	v_mov_b32_e32 v160, 0
	s_andn2_b64 vcc, exec, s[44:45]
	v_mov_b32_e32 v161, 0
	v_mov_b32_e32 v162, 0
	v_mov_b32_e32 v163, 0
	v_mov_b32_e32 v164, 0
	v_mov_b32_e32 v165, 0
	v_mov_b32_e32 v166, 0
	v_mov_b32_e32 v167, 0
	v_mov_b32_e32 v168, 0
	v_mov_b32_e32 v169, 0
	v_mov_b32_e32 v170, 0
	v_mov_b32_e32 v171, 0
	v_mov_b32_e32 v172, 0
	v_mov_b32_e32 v173, 0
	v_mov_b32_e32 v174, 0
	v_mov_b32_e32 v175, 0
	v_mov_b32_e32 v144, 0
	v_mov_b32_e32 v145, 0
	v_mov_b32_e32 v146, 0
	v_mov_b32_e32 v147, 0
	v_mov_b32_e32 v148, 0
	v_mov_b32_e32 v149, 0
	v_mov_b32_e32 v150, 0
	v_mov_b32_e32 v151, 0
	v_mov_b32_e32 v152, 0
	v_mov_b32_e32 v153, 0
	v_mov_b32_e32 v154, 0
	v_mov_b32_e32 v155, 0
	v_mov_b32_e32 v156, 0
	v_mov_b32_e32 v157, 0
	v_mov_b32_e32 v158, 0
	v_mov_b32_e32 v159, 0
	s_cbranch_vccnz .LBB0_200
	s_andn2_b64 vcc, exec, s[42:43]
	s_mov_b64 s[42:43], -1
	s_cbranch_vccnz .LBB0_198
	v_add_u32_e32 v144, 0x21780, v212
	v_add_u32_e32 v146, 0x21708, v212
	v_add_u32_e32 v147, 0x21788, v212
	v_add_u32_e32 v148, 0x21720, v212
	v_add_u32_e32 v149, 0x217a0, v212
	v_add_u32_e32 v150, 0x21728, v212
	v_add_u32_e32 v151, 0x217a8, v212
	v_add_u32_e32 v152, 0x21740, v212
	v_add_u32_e32 v153, 0x217c0, v212
	v_add_u32_e32 v154, 0x21748, v212
	v_add_u32_e32 v155, 0x217c8, v212
	v_add_u32_e32 v156, 0x21760, v212
	v_add_u32_e32 v157, 0x217e0, v212
	v_add_u32_e32 v158, 0x21768, v212
	v_add_u32_e32 v159, 0x217e8, v212
	ds_read2_b32 v[160:161], v213 offset1:1
	ds_read2_b32 v[144:145], v144 offset1:1
	ds_read2_b32 v[162:163], v146 offset1:1
	ds_read2_b32 v[146:147], v147 offset1:1
	ds_read2_b32 v[164:165], v148 offset1:1
	ds_read2_b32 v[148:149], v149 offset1:1
	ds_read2_b32 v[166:167], v150 offset1:1
	ds_read2_b32 v[150:151], v151 offset1:1
	ds_read2_b32 v[168:169], v152 offset1:1
	ds_read2_b32 v[152:153], v153 offset1:1
	ds_read2_b32 v[170:171], v154 offset1:1
	ds_read2_b32 v[154:155], v155 offset1:1
	ds_read2_b32 v[172:173], v156 offset1:1
	ds_read2_b32 v[156:157], v157 offset1:1
	ds_read2_b32 v[174:175], v158 offset1:1
	ds_read2_b32 v[158:159], v159 offset1:1
	s_mov_b64 s[42:43], 0

.LBB0_215:
	v_add_u32_e32 v212, s56, v225
	v_add_u32_e32 v6, v212, v227
	v_add_u32_e32 v7, v212, v228
	ds_read_b128 v[244:247], v6
	ds_read_b128 v[248:251], v6 offset:8192
	ds_read_b128 v[236:239], v7
	ds_read_b128 v[240:243], v7 offset:8192
	v_add_u32_e32 v6, v212, v229
	v_add_u32_e32 v7, v212, v230
	ds_read_b128 v[2:5], v6
	ds_read_b128 v[8:11], v6 offset:8192
	ds_read_b128 v[208:211], v7
	s_xor_b64 s[44:45], s[44:45], -1
	v_add_u32_e32 v6, v212, v226
	s_waitcnt lgkmcnt(6)
	v_mfma_f32_32x32x16_bf16 v[160:175], v[244:247], v[176:179], v[160:175]
	ds_read_b128 v[244:247], v7 offset:8192
	s_waitcnt lgkmcnt(6)
	v_mfma_f32_32x32x16_bf16 v[144:159], v[248:251], v[176:179], v[144:159]
	s_waitcnt lgkmcnt(5)
	v_mfma_f32_32x32x16_bf16 v[160:175], v[236:239], v[180:183], v[160:175]
	v_add_u32_e32 v7, v212, v231
	s_waitcnt lgkmcnt(4)
	v_mfma_f32_32x32x16_bf16 v[144:159], v[240:243], v[180:183], v[144:159]
	ds_read_b128 v[248:251], v6
	ds_read_b128 v[236:239], v6 offset:8192
	ds_read_b128 v[240:243], v7
	s_waitcnt lgkmcnt(6)
	v_mfma_f32_32x32x16_bf16 v[160:175], v[2:5], v[184:187], v[160:175]
	s_waitcnt lgkmcnt(5)
	v_mfma_f32_32x32x16_bf16 v[144:159], v[8:11], v[184:187], v[144:159]
	s_waitcnt lgkmcnt(4)
	v_mfma_f32_32x32x16_bf16 v[160:175], v[208:211], v[188:191], v[160:175]
	s_waitcnt lgkmcnt(3)
	v_mfma_f32_32x32x16_bf16 v[144:159], v[244:247], v[188:191], v[144:159]
	ds_read_b128 v[244:247], v7 offset:8192
	s_nop 9
	v_exp_f32_e32 v6, v160
	v_exp_f32_e32 v3, v161
	v_exp_f32_e32 v10, v164
	v_exp_f32_e32 v11, v165
	v_exp_f32_e32 v160, v172
	v_exp_f32_e32 v161, v173
	v_exp_f32_e32 v5, v162
	v_exp_f32_e32 v2, v144
	v_exp_f32_e32 v7, v146
	v_exp_f32_e32 v144, v148
	v_exp_f32_e32 v146, v150
	v_exp_f32_e32 v148, v168
	v_exp_f32_e32 v150, v169
	v_exp_f32_e32 v4, v145
	v_exp_f32_e32 v145, v149
	v_exp_f32_e32 v12, v166
	v_exp_f32_e32 v149, v152
	v_exp_f32_e32 v152, v170
	v_exp_f32_e32 v162, v174
	v_exp_f32_e32 v8, v163
	v_exp_f32_e32 v9, v147
	v_exp_f32_e32 v13, v167
	v_exp_f32_e32 v147, v151
	v_exp_f32_e32 v151, v153
	v_exp_f32_e32 v153, v154
	v_exp_f32_e32 v154, v171
	v_exp_f32_e32 v163, v175
	v_exp_f32_e32 v156, v156
	v_exp_f32_e32 v157, v157
	v_add_f32_e32 v164, v6, v3
	v_add_f32_e32 v165, v10, v11
	v_add_f32_e32 v166, v148, v150
	v_add_f32_e32 v167, v160, v161
	v_exp_f32_e32 v158, v158
	v_add_f32_e32 v164, v5, v164
	v_add_f32_e32 v165, v12, v165
	v_add_f32_e32 v166, v152, v166
	v_add_f32_e32 v167, v162, v167
	v_exp_f32_e32 v155, v155
	v_exp_f32_e32 v159, v159
	v_add_f32_e32 v164, v8, v164
	v_add_f32_e32 v165, v13, v165
	v_add_f32_e32 v166, v154, v166
	v_add_f32_e32 v167, v163, v167
	v_add_f32_e32 v164, v2, v164
	v_add_f32_e32 v165, v144, v165
	v_add_f32_e32 v166, v149, v166
	v_add_f32_e32 v167, v156, v167
	v_add_f32_e32 v164, v4, v164
	v_add_f32_e32 v165, v145, v165
	v_add_f32_e32 v166, v151, v166
	v_add_f32_e32 v167, v157, v167
	v_add_f32_e32 v164, v7, v164
	v_add_f32_e32 v165, v146, v165
	v_add_f32_e32 v166, v153, v166
	v_add_f32_e32 v167, v158, v167
	v_add_f32_e32 v164, v9, v164
	v_add_f32_e32 v165, v147, v165
	v_add_f32_e32 v166, v155, v166
	v_add_f32_e32 v167, v159, v167
	v_add_f32_e32 v164, v164, v165
	v_add_f32_e32 v165, v166, v167
	v_add_f32_e32 v213, v164, v165
	v_mov_b32_e32 v218, v213
	v_cvt_pk_bf16_f32 v208, v6, v3
	v_cvt_pk_bf16_f32 v209, v5, v8
	v_cvt_pk_bf16_f32 v210, v10, v11
	v_cvt_pk_bf16_f32 v211, v12, v13
	v_cvt_pk_bf16_f32 v10, v148, v150
	v_cvt_pk_bf16_f32 v11, v152, v154
	v_cvt_pk_bf16_f32 v12, v160, v161
	v_cvt_pk_bf16_f32 v13, v162, v163
	v_cvt_pk_bf16_f32 v6, v2, v4
	v_cvt_pk_bf16_f32 v7, v7, v9
	v_cvt_pk_bf16_f32 v8, v144, v145
	v_cvt_pk_bf16_f32 v9, v146, v147
	v_cvt_pk_bf16_f32 v2, v149, v151
	v_cvt_pk_bf16_f32 v3, v153, v155
	v_cvt_pk_bf16_f32 v4, v156, v157
	v_cvt_pk_bf16_f32 v5, v158, v159
	v_permlane32_swap_b32_e32 v213, v218
	v_permlane32_swap_b32_e32 v208, v210
	v_permlane32_swap_b32_e32 v209, v211
	v_permlane32_swap_b32_e32 v10, v12
	v_permlane32_swap_b32_e32 v11, v13
	v_permlane32_swap_b32_e32 v6, v8
	v_permlane32_swap_b32_e32 v7, v9
	v_permlane32_swap_b32_e32 v2, v4
	v_permlane32_swap_b32_e32 v3, v5
	s_nop 15
	s_nop 15
	v_mov_b32_e32 v160, 0
	s_andn2_b64 vcc, exec, s[44:45]
	v_mov_b32_e32 v161, 0
	v_mov_b32_e32 v162, 0
	v_mov_b32_e32 v163, 0
	v_mov_b32_e32 v164, 0
	v_mov_b32_e32 v165, 0
	v_mov_b32_e32 v166, 0
	v_mov_b32_e32 v167, 0
	v_mov_b32_e32 v168, 0
	v_mov_b32_e32 v169, 0
	v_mov_b32_e32 v170, 0
	v_mov_b32_e32 v171, 0
	v_mov_b32_e32 v172, 0
	v_mov_b32_e32 v173, 0
	v_mov_b32_e32 v174, 0
	v_mov_b32_e32 v175, 0
	v_mov_b32_e32 v144, 0
	v_mov_b32_e32 v145, 0
	v_mov_b32_e32 v146, 0
	v_mov_b32_e32 v147, 0
	v_mov_b32_e32 v148, 0
	v_mov_b32_e32 v149, 0
	v_mov_b32_e32 v150, 0
	v_mov_b32_e32 v151, 0
	v_mov_b32_e32 v152, 0
	v_mov_b32_e32 v153, 0
	v_mov_b32_e32 v154, 0
	v_mov_b32_e32 v155, 0
	v_mov_b32_e32 v156, 0
	v_mov_b32_e32 v157, 0
	v_mov_b32_e32 v158, 0
	v_mov_b32_e32 v159, 0
	s_cbranch_vccnz .LBB0_205
	s_andn2_b64 vcc, exec, s[42:43]
	s_mov_b64 s[42:43], -1
	s_cbranch_vccnz .LBB0_218
	v_add_u32_e32 v146, 0x21780, v219
	v_add_u32_e32 v147, 0x21708, v219
	v_add_u32_e32 v148, 0x21788, v219
	ds_read2_b32 v[144:145], v220 offset1:1
	ds_read2_b32 v[160:161], v146 offset1:1
	ds_read2_b32 v[146:147], v147 offset1:1
	ds_read2_b32 v[162:163], v148 offset1:1
	v_add_u32_e32 v148, 0x21720, v219
	v_add_u32_e32 v150, 0x217a0, v219
	v_add_u32_e32 v151, 0x21728, v219
	v_add_u32_e32 v152, 0x217a8, v219
	ds_read2_b32 v[148:149], v148 offset1:1
	ds_read2_b32 v[164:165], v150 offset1:1
	ds_read2_b32 v[150:151], v151 offset1:1
	ds_read2_b32 v[166:167], v152 offset1:1
	v_add_u32_e32 v152, 0x21740, v219
	v_add_u32_e32 v154, 0x217c0, v219
	v_add_u32_e32 v155, 0x21748, v219
	v_add_u32_e32 v156, 0x217c8, v219
	ds_read2_b32 v[152:153], v152 offset1:1
	ds_read2_b32 v[168:169], v154 offset1:1
	ds_read2_b32 v[154:155], v155 offset1:1
	ds_read2_b32 v[170:171], v156 offset1:1
	v_add_u32_e32 v156, 0x21760, v219
	v_add_u32_e32 v158, 0x217e0, v219
	v_add_u32_e32 v159, 0x21768, v219
	v_add_u32_e32 v174, 0x217e8, v219
	ds_read2_b32 v[156:157], v156 offset1:1
	ds_read2_b32 v[172:173], v158 offset1:1
	ds_read2_b32 v[158:159], v159 offset1:1
	ds_read2_b32 v[174:175], v174 offset1:1
	s_mov_b64 s[42:43], 0

.LBB0_286:
	s_or_b64 exec, exec, s[4:5]
	s_ashr_i32 s5, s7, 9
	s_and_b32 s24, s5, -2
	s_ashr_i32 s75, s7, 6
	s_lshr_b32 s5, 16, s24
	s_and_b32 s74, s6, 3
	s_ashr_i32 s4, s3, 3
	s_and_b32 s3, s75, 15
	s_sub_i32 s6, 4, s24
	s_add_i32 s5, s5, -1
	s_lshr_b32 s25, s3, s6
	s_and_b32 s3, s5, s3
	s_ashr_i32 s5, s4, 31
	s_lshl_b64 s[20:21], s[4:5], 12
	s_lshr_b32 s6, 0x400, s24
	s_or_b32 s4, s20, s25
	s_mul_i32 s6, s6, s74
	s_lshl_b32 s3, s3, 6
	s_mul_hi_u32 s26, s4, 0x1800
	s_mul_i32 s76, s21, 0x1800
	s_add_i32 s3, s3, s6
	s_lshl_b64 s[22:23], 8, s24
	s_mul_i32 s25, s4, 0x1800
	s_add_i32 s26, s26, s76
	s_add_u32 s25, s10, s25
	s_addc_u32 s26, s11, s26
	s_lshl_b32 s27, s16, 6
	s_lshl_b32 s16, s16, 7
	s_add_u32 s25, s25, s16
	v_sub_co_u32_e64 v2, s[6:7], s3, 64
	s_addc_u32 s26, s26, 0
	s_and_b64 s[6:7], s[6:7], exec
	v_readfirstlane_b32 s6, v2
	s_cselect_b32 s6, s3, s6
	s_ashr_i32 s7, s6, 31
	s_lshl_b64 s[6:7], s[6:7], s24
	v_bfe_u32 v3, v0, 3, 3
	s_mulk_i32 s7, 0x1800
	s_mul_hi_u32 s28, s6, 0x1800
	v_lshlrev_b32_e32 v3, s24, v3
	s_add_i32 s28, s28, s7
	s_mulk_i32 s6, 0x1800
	v_mul_lo_u32 v3, v3, s49
	v_lshlrev_b32_e32 v180, 3, v0
	s_add_u32 s6, s25, s6
	v_and_or_b32 v168, v180, 56, v3
	s_addc_u32 s7, s26, s28
	v_lshl_add_u64 v[2:3], v[168:169], 1, s[6:7]
	v_lshl_add_u64 v[4:5], v[2:3], 0, s[18:19]
	v_mad_u64_u32 v[6:7], s[6:7], s22, v172, v[4:5]
	s_mul_i32 s6, s23, 0x1800
	s_nop 0
	v_add_u32_e32 v7, s6, v7
	v_mad_u64_u32 v[8:9], s[6:7], s22, v173, v[4:5]
	s_mul_i32 s6, s23, 0x3000
	s_waitcnt lgkmcnt(0)
	s_barrier
	v_add_u32_e32 v9, s6, v9
	global_load_dwordx4 v[128:131], v[6:7], off
	global_load_dwordx4 v[132:135], v[8:9], off
	v_mad_u64_u32 v[6:7], s[6:7], s22, v174, v[4:5]
	s_mul_i32 s6, s23, 0x4800
	s_nop 0
	v_add_u32_e32 v7, s6, v7
	v_mad_u64_u32 v[8:9], s[6:7], s22, v175, v[4:5]
	s_mul_i32 s6, s23, 0x6000
	s_nop 0
	v_add_u32_e32 v9, s6, v9
	global_load_dwordx4 v[136:139], v[6:7], off
	global_load_dwordx4 v[140:143], v[8:9], off
	v_mad_u64_u32 v[6:7], s[6:7], s22, v176, v[4:5]
	s_mul_i32 s6, s23, 0x7800
	v_and_b32_e32 v1, 31, v0
	v_add_u32_e32 v7, s6, v7
	v_mad_u64_u32 v[8:9], s[6:7], s22, v177, v[4:5]
	s_mul_i32 s6, s23, 0x9000
	v_add_u32_e32 v168, s3, v1
	s_mov_b32 s5, s21
	v_add_u32_e32 v9, s6, v9
	global_load_dwordx4 v[144:147], v[6:7], off
	global_load_dwordx4 v[152:155], v[8:9], off
	v_mad_u64_u32 v[4:5], s[6:7], s22, v178, v[4:5]
	v_lshlrev_b64 v[6:7], s24, v[168:169]
	s_mul_i32 s6, s23, 0xa800
	v_lshl_add_u64 v[6:7], v[6:7], 0, s[4:5]
	v_add_u32_e32 v5, s6, v5
	v_mad_u64_u32 v[8:9], s[6:7], v6, s56, v[170:171]
	v_mov_b32_e32 v6, v9
	v_mad_u64_u32 v[6:7], s[6:7], v7, s56, v[6:7]
	v_add_co_u32_e32 v2, vcc, s57, v2
	v_mov_b32_e32 v9, v6
	v_lshrrev_b32_e32 v1, 1, v0
	v_addc_co_u32_e32 v3, vcc, 0, v3, vcc
	v_lshl_add_u64 v[6:7], v[8:9], 0, s[16:17]
	v_and_b32_e32 v8, 16, v1
	v_mov_b32_e32 v9, v169
	v_add_u32_e32 v168, 32, v168
	v_lshl_add_u64 v[6:7], v[6:7], 0, v[8:9]
	global_load_dwordx4 v[148:151], v[2:3], off
	global_load_dwordx4 v[96:99], v[6:7], off offset:3072
	global_load_dwordx4 v[100:103], v[6:7], off offset:3104
	global_load_dwordx4 v[104:107], v[6:7], off offset:3136
	v_lshlrev_b64 v[2:3], s24, v[168:169]
	v_lshl_add_u64 v[2:3], v[2:3], 0, s[4:5]
	v_mad_u64_u32 v[10:11], s[4:5], v2, s56, v[170:171]
	v_mov_b32_e32 v2, v11
	v_mad_u64_u32 v[2:3], s[4:5], v3, s56, v[2:3]
	v_mov_b32_e32 v11, v2
	v_lshl_add_u64 v[2:3], v[10:11], 0, s[16:17]
	v_lshl_add_u64 v[2:3], v[2:3], 0, v[8:9]
	global_load_dwordx4 v[108:111], v[6:7], off offset:3168
	global_load_dwordx4 v[112:115], v[2:3], off offset:3072
	global_load_dwordx4 v[116:119], v[2:3], off offset:3104
	global_load_dwordx4 v[120:123], v[2:3], off offset:3136
	global_load_dwordx4 v[156:159], v[4:5], off
	global_load_dwordx4 v[124:127], v[2:3], off offset:3168
	s_lshl_b32 s3, s75, 8
	s_lshl_b32 s4, s75, 13
	s_add_i32 s79, s4, 0
	s_add_i32 s81, s3, 0
	s_add_i32 s80, s79, 0x10000
	s_add_i32 s81, s81, 0x21000
	s_add_u32 s22, s10, s16
	v_and_b32_e32 v181, 63, v0
	s_mov_b32 s78, 0
	s_addc_u32 s23, s11, 0
	s_lshl_b32 s77, s27, 1
	s_cmp_lt_u32 s75, 4
	s_cbranch_scc1 .Ldil_nostag
	s_sleep 32
.Ldil_nostag:
	s_branch .LBB0_288
